# speedup vs baseline: 1.0051x; 1.0010x over previous
.LBB1_9:
	v_add_u32_e32 v182, s20, v209
	ds_read_b64_tr_b16 v[178:179], v182 offset:24576
	ds_read_b64_tr_b16 v[180:181], v182 offset:25088
	s_waitcnt lgkmcnt(9)
	v_mfma_f32_32x32x16_f16 v[98:113], v[174:177], v[142:145], v[34:49]
	s_mov_b64 s[2:3], 0
	v_add_f32_e32 v82, v66, v67
	v_add_f32_e32 v82, v68, v82
	v_add_f32_e32 v82, v69, v82
	v_add_f32_e32 v82, v70, v82
	v_add_f32_e32 v82, v71, v82
	v_cvt_pk_f16_f32 v134, v66, v67
	v_cvt_pk_f16_f32 v135, v68, v69
	ds_read_b64_tr_b16 v[174:175], v182 offset:28672
	ds_read_b64_tr_b16 v[176:177], v182 offset:29184
	v_add_f32_e32 v66, v72, v82
	s_waitcnt lgkmcnt(10)
	v_mfma_f32_32x32x16_f16 v[82:97], v[170:173], v[142:145], v[34:49]
	v_add_f32_e32 v66, v73, v66
	v_add_f32_e32 v66, v74, v66
	v_add_f32_e32 v66, v75, v66
	v_cvt_pk_f16_f32 v136, v70, v71
	v_cvt_pk_f16_f32 v137, v72, v73
	ds_read_b64_tr_b16 v[170:171], v182 offset:25600
	ds_read_b64_tr_b16 v[172:173], v182 offset:26112
	s_waitcnt lgkmcnt(11)
	v_mfma_f32_32x32x16_f16 v[98:113], v[166:169], v[138:141], v[98:113]
	v_add_f32_e32 v66, v76, v66
	v_add_f32_e32 v66, v77, v66
	v_add_f32_e32 v66, v78, v66
	v_add_f32_e32 v66, v79, v66
	v_cvt_pk_f16_f32 v126, v74, v75
	v_cvt_pk_f16_f32 v127, v76, v77
	ds_read_b64_tr_b16 v[74:75], v182 offset:29696
	ds_read_b64_tr_b16 v[76:77], v182 offset:30208
	s_waitcnt lgkmcnt(12)
	v_mfma_f32_32x32x16_f16 v[82:97], v[162:165], v[138:141], v[82:97]
	v_add_f32_e32 v66, v80, v66
	v_add_f32_e32 v66, v81, v66
	v_add_f32_e32 v66, v50, v66
	v_add_f32_e32 v66, v51, v66
	v_cvt_pk_f16_f32 v128, v78, v79
	v_cvt_pk_f16_f32 v129, v80, v81
	ds_read_b64_tr_b16 v[70:71], v182 offset:26624
	ds_read_b64_tr_b16 v[72:73], v182 offset:27136
	s_waitcnt lgkmcnt(13)
	v_mfma_f32_32x32x16_f16 v[98:113], v[158:161], v[130:133], v[98:113]
	v_add_f32_e32 v66, v52, v66
	v_add_f32_e32 v66, v53, v66
	v_add_f32_e32 v66, v54, v66
	v_add_f32_e32 v78, v55, v66
	v_cvt_pk_f16_f32 v118, v50, v51
	v_cvt_pk_f16_f32 v119, v52, v53
	ds_read_b64_tr_b16 v[66:67], v182 offset:30720
	ds_read_b64_tr_b16 v[68:69], v182 offset:31232
	s_waitcnt lgkmcnt(14)
	v_mfma_f32_32x32x16_f16 v[82:97], v[154:157], v[130:133], v[82:97]
	v_add_f32_e32 v50, v56, v78
	v_add_f32_e32 v50, v57, v50
	v_add_f32_e32 v50, v58, v50
	v_add_f32_e32 v50, v59, v50
	v_cvt_pk_f16_f32 v120, v54, v55
	v_cvt_pk_f16_f32 v121, v56, v57
	ds_read_b64_tr_b16 v[54:55], v182 offset:27648
	ds_read_b64_tr_b16 v[56:57], v182 offset:28160
	s_waitcnt lgkmcnt(14)
	v_mfma_f32_32x32x16_f16 v[98:113], v[150:153], v[122:125], v[98:113]
	v_add_f32_e32 v50, v60, v50
	v_add_f32_e32 v50, v61, v50
	v_add_f32_e32 v50, v62, v50
	v_add_f32_e32 v78, v63, v50
	v_cvt_pk_f16_f32 v114, v58, v59
	v_cvt_pk_f16_f32 v115, v60, v61
	ds_read_b64_tr_b16 v[50:51], v182 offset:31744
	ds_read_b64_tr_b16 v[52:53], v182 offset:32256
	v_mfma_f32_32x32x16_f16 v[82:97], v[146:149], v[122:125], v[82:97]
	v_add_f32_e32 v58, v64, v78
	v_add_f32_e32 v58, v65, v58
	v_cvt_pk_f16_f32 v116, v62, v63
	v_cvt_pk_f16_f32 v117, v64, v65
	v_max_f32_e32 v59, v98, v99
	v_max3_f32 v60, v100, v101, v102
	v_max3_f32 v59, v59, v103, v104
	v_max3_f32 v60, v60, v105, v106
	v_max3_f32 v59, v59, v107, v108
	v_max3_f32 v60, v60, v109, v110
	v_max3_f32 v59, v59, v111, v112
	v_add_f32_e32 v182, v203, v58
	v_max3_f32 v60, v60, v113, v82
	v_max3_f32 v59, v59, v83, v84
	v_max3_f32 v60, v60, v85, v86
	v_max3_f32 v59, v59, v87, v88
	v_max3_f32 v60, v60, v89, v90
	v_max3_f32 v59, v59, v91, v92
	v_max3_f32 v60, v60, v93, v94
	v_max3_f32 v59, v59, v95, v96
	v_max3_f32 v58, v59, v60, v97
	v_mov_b32_e32 v59, v58
	s_add_u32 s52, s16, 0xffffe000
	s_addc_u32 s53, s17, -1
	v_permlane32_swap_b32_e32 v58, v59
	v_max_f32_e32 v58, v58, v59
	v_cmp_lt_f32_e32 vcc, s23, v58
	s_cmp_lg_u64 vcc, 0
	s_cbranch_scc1 .LBB1_17

.LBB1_12:
	s_add_i32 s2, s22, 0x2000
	s_cmpk_lg_i32 s22, 0x4000
	s_cselect_b32 s43, s2, 0
	v_add_u32_e32 v183, s24, v209
	ds_read_b64_tr_b16 v[154:155], v183 offset:24576
	ds_read_b64_tr_b16 v[156:157], v183 offset:25088
	s_waitcnt lgkmcnt(9)
	v_mfma_f32_32x32x16_f16 v[66:81], v[58:61], v[142:145], v[34:49]
	s_mov_b64 s[2:3], 0
	v_add_f32_e32 v50, v98, v99
	v_add_f32_e32 v50, v100, v50
	v_add_f32_e32 v50, v101, v50
	v_add_f32_e32 v50, v102, v50
	v_add_f32_e32 v50, v103, v50
	v_cvt_pk_f16_f32 v134, v98, v99
	v_cvt_pk_f16_f32 v135, v100, v101
	ds_read_b64_tr_b16 v[150:151], v183 offset:28672
	ds_read_b64_tr_b16 v[152:153], v183 offset:29184
	v_add_f32_e32 v50, v104, v50
	v_add_f32_e32 v50, v105, v50
	v_add_f32_e32 v50, v106, v50
	v_add_f32_e32 v98, v107, v50
	s_waitcnt lgkmcnt(10)
	v_mfma_f32_32x32x16_f16 v[50:65], v[146:149], v[142:145], v[34:49]
	v_cvt_pk_f16_f32 v136, v102, v103
	v_cvt_pk_f16_f32 v137, v104, v105
	ds_read_b64_tr_b16 v[146:147], v183 offset:25600
	ds_read_b64_tr_b16 v[148:149], v183 offset:26112
	s_waitcnt lgkmcnt(11)
	v_mfma_f32_32x32x16_f16 v[66:81], v[178:181], v[138:141], v[66:81]
	v_add_f32_e32 v98, v108, v98
	v_add_f32_e32 v98, v109, v98
	v_add_f32_e32 v98, v110, v98
	v_add_f32_e32 v98, v111, v98
	v_cvt_pk_f16_f32 v126, v106, v107
	v_cvt_pk_f16_f32 v127, v108, v109
	ds_read_b64_tr_b16 v[106:107], v183 offset:29696
	ds_read_b64_tr_b16 v[108:109], v183 offset:30208
	s_waitcnt lgkmcnt(12)
	v_mfma_f32_32x32x16_f16 v[50:65], v[170:173], v[138:141], v[50:65]
	v_add_f32_e32 v98, v112, v98
	v_add_f32_e32 v98, v113, v98
	v_add_f32_e32 v98, v82, v98
	v_add_f32_e32 v98, v83, v98
	v_cvt_pk_f16_f32 v128, v110, v111
	v_cvt_pk_f16_f32 v129, v112, v113
	ds_read_b64_tr_b16 v[102:103], v183 offset:26624
	ds_read_b64_tr_b16 v[104:105], v183 offset:27136
	s_waitcnt lgkmcnt(13)
	v_mfma_f32_32x32x16_f16 v[66:81], v[174:177], v[130:133], v[66:81]
	v_add_f32_e32 v98, v84, v98
	v_add_f32_e32 v98, v85, v98
	v_add_f32_e32 v98, v86, v98
	v_add_f32_e32 v110, v87, v98
	v_cvt_pk_f16_f32 v118, v82, v83
	v_cvt_pk_f16_f32 v119, v84, v85
	ds_read_b64_tr_b16 v[98:99], v183 offset:30720
	ds_read_b64_tr_b16 v[100:101], v183 offset:31232
	s_waitcnt lgkmcnt(14)
	v_mfma_f32_32x32x16_f16 v[50:65], v[162:165], v[130:133], v[50:65]
	v_add_f32_e32 v82, v88, v110
	v_add_f32_e32 v82, v89, v82
	v_add_f32_e32 v82, v90, v82
	v_add_f32_e32 v82, v91, v82
	v_cvt_pk_f16_f32 v120, v86, v87
	v_cvt_pk_f16_f32 v121, v88, v89
	ds_read_b64_tr_b16 v[86:87], v183 offset:27648
	ds_read_b64_tr_b16 v[88:89], v183 offset:28160
	s_waitcnt lgkmcnt(14)
	v_mfma_f32_32x32x16_f16 v[66:81], v[166:169], v[122:125], v[66:81]
	v_add_f32_e32 v82, v92, v82
	v_add_f32_e32 v82, v93, v82
	v_add_f32_e32 v82, v94, v82
	v_add_f32_e32 v110, v95, v82
	v_cvt_pk_f16_f32 v114, v90, v91
	v_cvt_pk_f16_f32 v115, v92, v93
	ds_read_b64_tr_b16 v[82:83], v183 offset:31744
	ds_read_b64_tr_b16 v[84:85], v183 offset:32256
	v_mfma_f32_32x32x16_f16 v[50:65], v[158:161], v[122:125], v[50:65]
	v_add_f32_e32 v90, v96, v110
	v_add_f32_e32 v90, v97, v90
	v_cvt_pk_f16_f32 v116, v94, v95
	v_cvt_pk_f16_f32 v117, v96, v97
	v_max_f32_e32 v91, v66, v67
	v_max3_f32 v92, v68, v69, v70
	v_max3_f32 v91, v91, v71, v72
	v_max3_f32 v92, v92, v73, v74
	v_max3_f32 v91, v91, v75, v76
	v_max3_f32 v92, v92, v77, v78
	v_max3_f32 v91, v91, v79, v80
	v_add_f32_e32 v203, v182, v90
	v_max3_f32 v92, v92, v81, v50
	v_max3_f32 v91, v91, v51, v52
	v_max3_f32 v92, v92, v53, v54
	v_max3_f32 v91, v91, v55, v56
	v_max3_f32 v92, v92, v57, v58
	v_max3_f32 v91, v91, v59, v60
	v_max3_f32 v92, v92, v61, v62
	v_max3_f32 v91, v91, v63, v64
	v_max3_f32 v90, v91, v92, v65
	v_mov_b32_e32 v91, v90
	s_add_u32 s52, s18, 0x2000
	s_addc_u32 s53, s19, 0
	v_permlane32_swap_b32_e32 v90, v91
	v_max_f32_e32 v90, v90, v91
	v_cmp_lt_f32_e32 vcc, s23, v90
	s_cmp_lg_u64 vcc, 0
	s_cbranch_scc1 .LBB1_20

.LBB1_17:
	s_mov_b64 s[2:3], -1
	v_max_f32_e32 v34, v58, v58
	v_max_f32_e32 v58, 0, v34
	v_exp_f32_e64 v59, -v58
	v_add_f32_e32 v199, v199, v58
	v_xor_b32_e32 v34, 0x80000000, v199
	v_mov_b32_e32 v35, v34
	v_mov_b32_e32 v36, v34
	v_mov_b32_e32 v37, v34
	v_mov_b32_e32 v38, v34
	v_mov_b32_e32 v39, v34
	v_mov_b32_e32 v40, v34
	v_mov_b32_e32 v41, v34
	v_mov_b32_e32 v42, v34
	v_mov_b32_e32 v43, v34
	v_mov_b32_e32 v44, v34
	v_mov_b32_e32 v45, v34
	v_mov_b32_e32 v46, v34
	v_mov_b32_e32 v47, v34
	v_mov_b32_e32 v48, v34
	v_mov_b32_e32 v49, v34
	s_and_saveexec_b64 s[20:21], s[0:1]
	ds_write_b32 v198, v59 offset:49152
	s_or_b64 exec, exec, s[20:21]
	v_sub_f32_e32 v113, v113, v58
	v_sub_f32_e32 v112, v112, v58
	v_sub_f32_e32 v111, v111, v58
	v_sub_f32_e32 v110, v110, v58
	v_sub_f32_e32 v109, v109, v58
	v_sub_f32_e32 v108, v108, v58
	v_sub_f32_e32 v107, v107, v58
	v_sub_f32_e32 v106, v106, v58
	v_sub_f32_e32 v105, v105, v58
	v_sub_f32_e32 v104, v104, v58
	v_sub_f32_e32 v103, v103, v58
	v_sub_f32_e32 v102, v102, v58
	v_sub_f32_e32 v101, v101, v58
	v_sub_f32_e32 v100, v100, v58
	v_sub_f32_e32 v99, v99, v58
	v_sub_f32_e32 v98, v98, v58
	v_sub_f32_e32 v97, v97, v58
	v_sub_f32_e32 v96, v96, v58
	v_sub_f32_e32 v95, v95, v58
	v_sub_f32_e32 v94, v94, v58
	v_sub_f32_e32 v93, v93, v58
	v_sub_f32_e32 v92, v92, v58
	v_sub_f32_e32 v91, v91, v58
	v_sub_f32_e32 v90, v90, v58
	v_sub_f32_e32 v89, v89, v58
	v_sub_f32_e32 v88, v88, v58
	v_sub_f32_e32 v87, v87, v58
	v_sub_f32_e32 v86, v86, v58
	v_sub_f32_e32 v85, v85, v58
	v_sub_f32_e32 v84, v84, v58
	v_sub_f32_e32 v83, v83, v58
	v_sub_f32_e32 v82, v82, v58
	v_mul_f32_e32 v182, v182, v59
	s_branch .LBB1_10
.LBB1_20:
	s_mov_b64 s[2:3], -1
	v_max_f32_e32 v34, v90, v90
	v_max_f32_e32 v90, 0, v34
	v_exp_f32_e64 v91, -v90
	v_add_f32_e32 v199, v199, v90
	v_xor_b32_e32 v34, 0x80000000, v199
	v_mov_b32_e32 v35, v34
	v_mov_b32_e32 v36, v34
	v_mov_b32_e32 v37, v34
	v_mov_b32_e32 v38, v34
	v_mov_b32_e32 v39, v34
	v_mov_b32_e32 v40, v34
	v_mov_b32_e32 v41, v34
	v_mov_b32_e32 v42, v34
	v_mov_b32_e32 v43, v34
	v_mov_b32_e32 v44, v34
	v_mov_b32_e32 v45, v34
	v_mov_b32_e32 v46, v34
	v_mov_b32_e32 v47, v34
	v_mov_b32_e32 v48, v34
	v_mov_b32_e32 v49, v34
	s_and_saveexec_b64 s[20:21], s[0:1]
	ds_write_b32 v198, v91 offset:49152
	s_or_b64 exec, exec, s[20:21]
	v_sub_f32_e32 v81, v81, v90
	v_sub_f32_e32 v80, v80, v90
	v_sub_f32_e32 v79, v79, v90
	v_sub_f32_e32 v78, v78, v90
	v_sub_f32_e32 v77, v77, v90
	v_sub_f32_e32 v76, v76, v90
	v_sub_f32_e32 v75, v75, v90
	v_sub_f32_e32 v74, v74, v90
	v_sub_f32_e32 v73, v73, v90
	v_sub_f32_e32 v72, v72, v90
	v_sub_f32_e32 v71, v71, v90
	v_sub_f32_e32 v70, v70, v90
	v_sub_f32_e32 v69, v69, v90
	v_sub_f32_e32 v68, v68, v90
	v_sub_f32_e32 v67, v67, v90
	v_sub_f32_e32 v66, v66, v90
	v_sub_f32_e32 v65, v65, v90
	v_sub_f32_e32 v64, v64, v90
	v_sub_f32_e32 v63, v63, v90
	v_sub_f32_e32 v62, v62, v90
	v_sub_f32_e32 v61, v61, v90
	v_sub_f32_e32 v60, v60, v90
	v_sub_f32_e32 v59, v59, v90
	v_sub_f32_e32 v58, v58, v90
	v_sub_f32_e32 v57, v57, v90
	v_sub_f32_e32 v56, v56, v90
	v_sub_f32_e32 v55, v55, v90
	v_sub_f32_e32 v54, v54, v90
	v_sub_f32_e32 v53, v53, v90
	v_sub_f32_e32 v52, v52, v90
	v_sub_f32_e32 v51, v51, v90
	v_sub_f32_e32 v50, v50, v90
	v_mul_f32_e32 v203, v203, v91
	s_branch .LBB1_13

.LBB1_87:
	v_add_u32_e32 v65, s6, v251
	ds_read_b64_tr_b16 v[192:193], v65
	ds_read_b64_tr_b16 v[194:195], v65 offset:512
	s_waitcnt lgkmcnt(9)
	v_mfma_f32_32x32x16_f16 v[112:127], v[188:191], v[140:143], v[32:47]
	s_mov_b64 s[6:7], 0
	v_add_f32_e32 v66, v80, v81
	v_add_f32_e32 v66, v82, v66
	v_add_f32_e32 v66, v83, v66
	v_add_f32_e32 v66, v84, v66
	v_add_f32_e32 v66, v85, v66
	v_cvt_pk_f16_f32 v156, v80, v81
	v_cvt_pk_f16_f32 v157, v82, v83
	ds_read_b64_tr_b16 v[188:189], v65 offset:4096
	ds_read_b64_tr_b16 v[190:191], v65 offset:4608
	s_waitcnt lgkmcnt(10)
	v_mfma_f32_32x32x16_f16 v[96:111], v[184:187], v[140:143], v[32:47]
	v_add_f32_e32 v66, v86, v66
	v_add_f32_e32 v66, v87, v66
	v_add_f32_e32 v66, v88, v66
	v_add_f32_e32 v66, v89, v66
	v_cvt_pk_f16_f32 v158, v84, v85
	v_cvt_pk_f16_f32 v159, v86, v87
	ds_read_b64_tr_b16 v[78:79], v65 offset:1024
	ds_read_b64_tr_b16 v[80:81], v65 offset:1536
	s_waitcnt lgkmcnt(11)
	v_mfma_f32_32x32x16_f16 v[112:127], v[180:183], v[136:139], v[112:127]
	v_add_f32_e32 v66, v90, v66
	v_add_f32_e32 v66, v91, v66
	v_add_f32_e32 v66, v92, v66
	v_add_f32_e32 v66, v93, v66
	v_cvt_pk_f16_f32 v152, v88, v89
	v_cvt_pk_f16_f32 v153, v90, v91
	ds_read_b64_tr_b16 v[74:75], v65 offset:5120
	ds_read_b64_tr_b16 v[76:77], v65 offset:5632
	s_waitcnt lgkmcnt(12)
	v_mfma_f32_32x32x16_f16 v[96:111], v[176:179], v[136:139], v[96:111]
	v_add_f32_e32 v66, v94, v66
	v_add_f32_e32 v66, v95, v66
	v_add_f32_e32 v66, v48, v66
	v_add_f32_e32 v66, v49, v66
	v_cvt_pk_f16_f32 v154, v92, v93
	v_cvt_pk_f16_f32 v155, v94, v95
	ds_read_b64_tr_b16 v[70:71], v65 offset:2048
	ds_read_b64_tr_b16 v[72:73], v65 offset:2560
	s_waitcnt lgkmcnt(13)
	v_mfma_f32_32x32x16_f16 v[112:127], v[172:175], v[132:135], v[112:127]
	v_add_f32_e32 v66, v50, v66
	v_add_f32_e32 v66, v51, v66
	v_add_f32_e32 v66, v52, v66
	v_add_f32_e32 v82, v53, v66
	v_cvt_pk_f16_f32 v148, v48, v49
	v_cvt_pk_f16_f32 v149, v50, v51
	ds_read_b64_tr_b16 v[66:67], v65 offset:6144
	ds_read_b64_tr_b16 v[68:69], v65 offset:6656
	s_waitcnt lgkmcnt(14)
	v_mfma_f32_32x32x16_f16 v[96:111], v[168:171], v[132:135], v[96:111]
	v_add_f32_e32 v48, v54, v82
	v_add_f32_e32 v48, v55, v48
	v_add_f32_e32 v48, v56, v48
	v_add_f32_e32 v48, v57, v48
	v_cvt_pk_f16_f32 v150, v52, v53
	v_cvt_pk_f16_f32 v151, v54, v55
	ds_read_b64_tr_b16 v[52:53], v65 offset:3072
	ds_read_b64_tr_b16 v[54:55], v65 offset:3584
	s_waitcnt lgkmcnt(14)
	v_mfma_f32_32x32x16_f16 v[112:127], v[164:167], v[128:131], v[112:127]
	v_add_f32_e32 v48, v58, v48
	v_add_f32_e32 v48, v59, v48
	v_add_f32_e32 v48, v60, v48
	v_add_f32_e32 v82, v61, v48
	v_cvt_pk_f16_f32 v144, v56, v57
	v_cvt_pk_f16_f32 v145, v58, v59
	ds_read_b64_tr_b16 v[48:49], v65 offset:7168
	ds_read_b64_tr_b16 v[50:51], v65 offset:7680
	v_mfma_f32_32x32x16_f16 v[96:111], v[160:163], v[128:131], v[96:111]
	v_add_f32_e32 v56, v62, v82
	v_add_f32_e32 v56, v63, v56
	v_cvt_pk_f16_f32 v146, v60, v61
	v_cvt_pk_f16_f32 v147, v62, v63
	v_max_f32_e32 v57, v112, v113
	v_max3_f32 v58, v114, v115, v116
	v_max3_f32 v57, v57, v117, v118
	v_max3_f32 v58, v58, v119, v120
	v_max3_f32 v57, v57, v121, v122
	v_max3_f32 v58, v58, v123, v124
	v_max3_f32 v57, v57, v125, v126
	v_add_f32_e32 v64, v64, v56
	v_max3_f32 v58, v58, v127, v96
	v_max3_f32 v57, v57, v97, v98
	v_max3_f32 v58, v58, v99, v100
	v_max3_f32 v57, v57, v101, v102
	v_max3_f32 v58, v58, v103, v104
	v_max3_f32 v57, v57, v105, v106
	v_max3_f32 v58, v58, v107, v108
	v_max3_f32 v57, v57, v109, v110
	v_max3_f32 v56, v57, v58, v111
	v_mov_b32_e32 v57, v56
	s_add_u32 s52, s4, 0xffffe000
	s_addc_u32 s53, s5, -1
	v_permlane32_swap_b32_e32 v56, v57
	v_max_f32_e32 v56, v56, v57
	v_cmp_lt_f32_e32 vcc, s17, v56
	s_cmp_lg_u64 vcc, 0
	s_cbranch_scc1 .LBB1_95

.LBB1_90:
	s_add_i32 s6, s12, 0x2000
	s_cmpk_lg_i32 s12, 0x4000
	s_cselect_b32 s25, s6, 0
	v_add_u32_e32 v65, s30, v251
	ds_read_b64_tr_b16 v[168:169], v65
	ds_read_b64_tr_b16 v[170:171], v65 offset:512
	s_waitcnt lgkmcnt(9)
	v_mfma_f32_32x32x16_f16 v[80:95], v[56:59], v[140:143], v[32:47]
	s_mov_b64 s[6:7], 0
	v_add_f32_e32 v48, v112, v113
	v_add_f32_e32 v48, v114, v48
	v_add_f32_e32 v48, v115, v48
	v_add_f32_e32 v48, v116, v48
	v_add_f32_e32 v48, v117, v48
	v_cvt_pk_f16_f32 v156, v112, v113
	v_cvt_pk_f16_f32 v157, v114, v115
	ds_read_b64_tr_b16 v[164:165], v65 offset:4096
	ds_read_b64_tr_b16 v[166:167], v65 offset:4608
	v_add_f32_e32 v48, v118, v48
	v_add_f32_e32 v48, v119, v48
	v_add_f32_e32 v48, v120, v48
	v_add_f32_e32 v66, v121, v48
	s_waitcnt lgkmcnt(10)
	v_mfma_f32_32x32x16_f16 v[48:63], v[160:163], v[140:143], v[32:47]
	v_cvt_pk_f16_f32 v158, v116, v117
	v_cvt_pk_f16_f32 v159, v118, v119
	ds_read_b64_tr_b16 v[160:161], v65 offset:1024
	ds_read_b64_tr_b16 v[162:163], v65 offset:1536
	s_waitcnt lgkmcnt(11)
	v_mfma_f32_32x32x16_f16 v[80:95], v[188:191], v[136:139], v[80:95]
	v_add_f32_e32 v66, v122, v66
	v_add_f32_e32 v66, v123, v66
	v_add_f32_e32 v66, v124, v66
	v_add_f32_e32 v66, v125, v66
	v_cvt_pk_f16_f32 v152, v120, v121
	v_cvt_pk_f16_f32 v153, v122, v123
	ds_read_b64_tr_b16 v[116:117], v65 offset:5120
	ds_read_b64_tr_b16 v[118:119], v65 offset:5632
	s_waitcnt lgkmcnt(12)
	v_mfma_f32_32x32x16_f16 v[48:63], v[184:187], v[136:139], v[48:63]
	v_add_f32_e32 v66, v126, v66
	v_add_f32_e32 v66, v127, v66
	v_add_f32_e32 v66, v96, v66
	v_add_f32_e32 v66, v97, v66
	v_cvt_pk_f16_f32 v154, v124, v125
	v_cvt_pk_f16_f32 v155, v126, v127
	ds_read_b64_tr_b16 v[112:113], v65 offset:2048
	ds_read_b64_tr_b16 v[114:115], v65 offset:2560
	s_waitcnt lgkmcnt(13)
	v_mfma_f32_32x32x16_f16 v[80:95], v[74:77], v[132:135], v[80:95]
	v_add_f32_e32 v66, v98, v66
	v_add_f32_e32 v66, v99, v66
	v_add_f32_e32 v66, v100, v66
	v_add_f32_e32 v66, v101, v66
	v_cvt_pk_f16_f32 v148, v96, v97
	v_cvt_pk_f16_f32 v149, v98, v99
	ds_read_b64_tr_b16 v[74:75], v65 offset:6144
	ds_read_b64_tr_b16 v[76:77], v65 offset:6656
	s_waitcnt lgkmcnt(14)
	v_mfma_f32_32x32x16_f16 v[48:63], v[176:179], v[132:135], v[48:63]
	v_add_f32_e32 v66, v102, v66
	v_add_f32_e32 v66, v103, v66
	v_add_f32_e32 v66, v104, v66
	v_add_f32_e32 v66, v105, v66
	v_cvt_pk_f16_f32 v150, v100, v101
	v_cvt_pk_f16_f32 v151, v102, v103
	ds_read_b64_tr_b16 v[70:71], v65 offset:3072
	ds_read_b64_tr_b16 v[72:73], v65 offset:3584
	s_waitcnt lgkmcnt(14)
	v_mfma_f32_32x32x16_f16 v[80:95], v[180:183], v[128:131], v[80:95]
	v_add_f32_e32 v66, v106, v66
	v_add_f32_e32 v66, v107, v66
	v_add_f32_e32 v66, v108, v66
	v_add_f32_e32 v78, v109, v66
	v_cvt_pk_f16_f32 v144, v104, v105
	v_cvt_pk_f16_f32 v145, v106, v107
	ds_read_b64_tr_b16 v[66:67], v65 offset:7168
	ds_read_b64_tr_b16 v[68:69], v65 offset:7680
	v_mfma_f32_32x32x16_f16 v[48:63], v[172:175], v[128:131], v[48:63]
	v_add_f32_e32 v65, v110, v78
	v_add_f32_e32 v65, v111, v65
	v_cvt_pk_f16_f32 v146, v108, v109
	v_cvt_pk_f16_f32 v147, v110, v111
	v_max_f32_e32 v78, v80, v81
	v_max3_f32 v79, v82, v83, v84
	v_max3_f32 v78, v78, v85, v86
	v_max3_f32 v79, v79, v87, v88
	v_max3_f32 v78, v78, v89, v90
	v_max3_f32 v79, v79, v91, v92
	v_max3_f32 v78, v78, v93, v94
	v_add_f32_e32 v64, v64, v65
	v_max3_f32 v79, v79, v95, v48
	v_max3_f32 v78, v78, v49, v50
	v_max3_f32 v79, v79, v51, v52
	v_max3_f32 v78, v78, v53, v54
	v_max3_f32 v79, v79, v55, v56
	v_max3_f32 v78, v78, v57, v58
	v_max3_f32 v79, v79, v59, v60
	v_max3_f32 v78, v78, v61, v62
	v_max3_f32 v65, v78, v79, v63
	v_mov_b32_e32 v78, v65
	s_add_i32 s54, s12, s22
	s_add_i32 s55, s25, s23
	v_permlane32_swap_b32_e32 v65, v78
	v_max_f32_e32 v65, v65, v78
	v_cmp_lt_f32_e32 vcc, s17, v65
	s_cmp_lg_u64 vcc, 0
	s_cbranch_scc1 .LBB1_98

.LBB1_95:
	s_mov_b64 s[6:7], -1
	v_max_f32_e32 v32, v56, v56
	v_max_f32_e32 v56, 0, v32
	v_exp_f32_e64 v57, -v56
	v_add_f32_e32 v249, v249, v56
	v_xor_b32_e32 v32, 0x80000000, v249
	v_mov_b32_e32 v33, v32
	v_mov_b32_e32 v34, v32
	v_mov_b32_e32 v35, v32
	v_mov_b32_e32 v36, v32
	v_mov_b32_e32 v37, v32
	v_mov_b32_e32 v38, v32
	v_mov_b32_e32 v39, v32
	v_mov_b32_e32 v40, v32
	v_mov_b32_e32 v41, v32
	v_mov_b32_e32 v42, v32
	v_mov_b32_e32 v43, v32
	v_mov_b32_e32 v44, v32
	v_mov_b32_e32 v45, v32
	v_mov_b32_e32 v46, v32
	v_mov_b32_e32 v47, v32
	s_and_saveexec_b64 s[8:9], s[0:1]
	ds_write_b32 v205, v57 offset:49152
	s_or_b64 exec, exec, s[8:9]
	v_sub_f32_e32 v127, v127, v56
	v_sub_f32_e32 v126, v126, v56
	v_sub_f32_e32 v125, v125, v56
	v_sub_f32_e32 v124, v124, v56
	v_sub_f32_e32 v123, v123, v56
	v_sub_f32_e32 v122, v122, v56
	v_sub_f32_e32 v121, v121, v56
	v_sub_f32_e32 v120, v120, v56
	v_sub_f32_e32 v119, v119, v56
	v_sub_f32_e32 v118, v118, v56
	v_sub_f32_e32 v117, v117, v56
	v_sub_f32_e32 v116, v116, v56
	v_sub_f32_e32 v115, v115, v56
	v_sub_f32_e32 v114, v114, v56
	v_sub_f32_e32 v113, v113, v56
	v_sub_f32_e32 v112, v112, v56
	v_sub_f32_e32 v111, v111, v56
	v_sub_f32_e32 v110, v110, v56
	v_sub_f32_e32 v109, v109, v56
	v_sub_f32_e32 v108, v108, v56
	v_sub_f32_e32 v107, v107, v56
	v_sub_f32_e32 v106, v106, v56
	v_sub_f32_e32 v105, v105, v56
	v_sub_f32_e32 v104, v104, v56
	v_sub_f32_e32 v103, v103, v56
	v_sub_f32_e32 v102, v102, v56
	v_sub_f32_e32 v101, v101, v56
	v_sub_f32_e32 v100, v100, v56
	v_sub_f32_e32 v99, v99, v56
	v_sub_f32_e32 v98, v98, v56
	v_sub_f32_e32 v97, v97, v56
	v_sub_f32_e32 v96, v96, v56
	v_mul_f32_e32 v64, v64, v57
	s_branch .LBB1_88
.LBB1_98:
	s_mov_b64 s[6:7], -1
	v_max_f32_e32 v32, v65, v65
	v_max_f32_e32 v65, 0, v32
	v_exp_f32_e64 v78, -v65
	v_add_f32_e32 v249, v249, v65
	v_xor_b32_e32 v32, 0x80000000, v249
	v_mov_b32_e32 v33, v32
	v_mov_b32_e32 v34, v32
	v_mov_b32_e32 v35, v32
	v_mov_b32_e32 v36, v32
	v_mov_b32_e32 v37, v32
	v_mov_b32_e32 v38, v32
	v_mov_b32_e32 v39, v32
	v_mov_b32_e32 v40, v32
	v_mov_b32_e32 v41, v32
	v_mov_b32_e32 v42, v32
	v_mov_b32_e32 v43, v32
	v_mov_b32_e32 v44, v32
	v_mov_b32_e32 v45, v32
	v_mov_b32_e32 v46, v32
	v_mov_b32_e32 v47, v32
	s_and_saveexec_b64 s[8:9], s[0:1]
	ds_write_b32 v205, v78 offset:49152
	s_or_b64 exec, exec, s[8:9]
	v_sub_f32_e32 v95, v95, v65
	v_sub_f32_e32 v94, v94, v65
	v_sub_f32_e32 v93, v93, v65
	v_sub_f32_e32 v92, v92, v65
	v_sub_f32_e32 v91, v91, v65
	v_sub_f32_e32 v90, v90, v65
	v_sub_f32_e32 v89, v89, v65
	v_sub_f32_e32 v88, v88, v65
	v_sub_f32_e32 v87, v87, v65
	v_sub_f32_e32 v86, v86, v65
	v_sub_f32_e32 v85, v85, v65
	v_sub_f32_e32 v84, v84, v65
	v_sub_f32_e32 v83, v83, v65
	v_sub_f32_e32 v82, v82, v65
	v_sub_f32_e32 v81, v81, v65
	v_sub_f32_e32 v80, v80, v65
	v_sub_f32_e32 v63, v63, v65
	v_sub_f32_e32 v62, v62, v65
	v_sub_f32_e32 v61, v61, v65
	v_sub_f32_e32 v60, v60, v65
	v_sub_f32_e32 v59, v59, v65
	v_sub_f32_e32 v58, v58, v65
	v_sub_f32_e32 v57, v57, v65
	v_sub_f32_e32 v56, v56, v65
	v_sub_f32_e32 v55, v55, v65
	v_sub_f32_e32 v54, v54, v65
	v_sub_f32_e32 v53, v53, v65
	v_sub_f32_e32 v52, v52, v65
	v_sub_f32_e32 v51, v51, v65
	v_sub_f32_e32 v50, v50, v65
	v_sub_f32_e32 v49, v49, v65
	v_sub_f32_e32 v48, v48, v65
	v_mul_f32_e32 v64, v64, v78
	s_branch .LBB1_91
